# speedup vs baseline: 1.0024x; 1.0005x over previous
_Z12fused_kernel6Params:
	s_load_dwordx16 s[52:67], s[0:1], 0x0
	s_load_dwordx16 s[36:51], s[0:1], 0x40
	s_load_dwordx16 s[8:23], s[0:1], 0x80
	s_load_dwordx4 s[24:27], s[0:1], 0xc0
	s_and_b32 s3, s2, 0x7f
	s_cmpk_gt_u32 s2, 0x7f
	v_and_b32_e32 v80, 63, v0
	s_mov_b64 s[0:1], -1
	s_mul_i32 s33, s3, 0x1c20
	s_cbranch_scc0 .Lk_217
	s_sleep 40
	v_readfirstlane_b32 s4, v0
	s_cmpk_lt_u32 s4, 0x300
	s_cbranch_scc1 .Lk_3
	s_setprio 1
